# baseline (speedup 1.0000x reference)
_Z5k_aggILi1EEvPKDF16_PKiPKjPKfS7_S1_PDF16_Pf:
	s_and_b32 s3, s2, 7
	s_lshr_b32 s2, s2, 3
	s_mul_i32 s12, s3, 0x186
	s_min_u32 s3, s3, 5
	s_load_dwordx8 s[4:11], s[0:1], 0x0
	s_add_i32 s2, s3, s2
	v_lshrrev_b32_e32 v1, 6, v0
	v_bfe_u32 v2, v0, 3, 3
	s_add_i32 s2, s2, s12
	v_lshl_or_b32 v16, v1, 3, v2
	s_lshl_b32 s12, s2, 5
	v_or_b32_e32 v10, s12, v16
	v_mov_b32_e32 v11, 0
	v_lshlrev_b64 v[2:3], 2, v[10:11]
	s_waitcnt lgkmcnt(0)
	v_lshl_add_u64 v[4:5], s[6:7], 0, v[2:3]
	global_load_dwordx2 v[12:13], v[4:5], off
	v_and_b32_e32 v17, 7, v0
	v_lshlrev_b64 v[4:5], 7, v[10:11]
	v_lshlrev_b32_e32 v10, 4, v17
	v_lshl_add_u64 v[4:5], s[4:5], 0, v[4:5]
	v_lshl_add_u64 v[4:5], v[4:5], 0, v[10:11]
	global_load_dwordx4 v[24:27], v[4:5], off
	v_lshl_add_u64 v[4:5], s[10:11], 0, v[2:3]
	s_load_dwordx2 s[2:3], s[0:1], 0x20
	s_waitcnt vmcnt(1)
	v_ashrrev_i32_e32 v3, 31, v12
	v_mov_b32_e32 v2, v12
	v_lshl_add_u64 v[2:3], v[2:3], 2, s[8:9]
	global_load_dwordx3 v[6:8], v[2:3], off
	global_load_dword v18, v[4:5], off
	v_add_u32_e32 v4, 4, v12
	v_cmp_le_i32_e32 vcc, v4, v13
	s_waitcnt vmcnt(2)
	v_cvt_f32_f16_e32 v19, v24
	v_cvt_f32_f16_sdwa v20, v24 dst_sel:DWORD dst_unused:UNUSED_PAD src0_sel:WORD_1
	v_cvt_f32_f16_e32 v21, v25
	v_cvt_f32_f16_sdwa v22, v25 dst_sel:DWORD dst_unused:UNUSED_PAD src0_sel:WORD_1
	v_cvt_f32_f16_e32 v23, v26
	v_cvt_f32_f16_sdwa v24, v26 dst_sel:DWORD dst_unused:UNUSED_PAD src0_sel:WORD_1
	v_cvt_f32_f16_e32 v25, v27
	v_cvt_f32_f16_sdwa v26, v27 dst_sel:DWORD dst_unused:UNUSED_PAD src0_sel:WORD_1
	s_and_saveexec_b64 s[6:7], vcc
	s_cbranch_execz .LBB2_4
	global_load_dword v11, v[2:3], off offset:12
	v_lshl_add_u64 v[14:15], v[2:3], 0, 16
	s_mov_b64 s[8:9], 0
	s_mov_b32 s10, 0xffff8
	v_mov_b32_e32 v9, -2
	.p2alignl 6, 3212836864

_Z5k_aggILi2EEvPKDF16_PKiPKjPKfS7_S1_PDF16_Pf:
	s_and_b32 s3, s2, 7
	s_load_dwordx8 s[4:11], s[0:1], 0x0
	s_lshr_b32 s2, s2, 3
	s_mul_i32 s12, s3, 0x186
	s_min_u32 s3, s3, 5
	s_add_i32 s2, s3, s2
	v_lshrrev_b32_e32 v1, 3, v0
	s_add_i32 s2, s2, s12
	v_lshl_or_b32 v4, s2, 5, v1
	v_mov_b32_e32 v5, 0
	v_lshlrev_b64 v[6:7], 2, v[4:5]
	s_waitcnt lgkmcnt(0)
	v_lshl_add_u64 v[2:3], s[6:7], 0, v[6:7]
	global_load_dwordx2 v[18:19], v[2:3], off
	v_and_b32_e32 v3, 7, v0
	v_lshlrev_b64 v[0:1], 7, v[4:5]
	v_mov_b32_e32 v9, v5
	v_lshlrev_b32_e32 v8, 4, v3
	v_lshl_add_u64 v[0:1], s[4:5], 0, v[0:1]
	v_lshl_add_u64 v[0:1], v[0:1], 0, v[8:9]
	global_load_dwordx4 v[22:25], v[0:1], off
	v_lshl_add_u64 v[10:11], s[10:11], 0, v[6:7]
	s_waitcnt vmcnt(1)
	v_ashrrev_i32_e32 v1, 31, v18
	v_mov_b32_e32 v0, v18
	v_lshl_add_u64 v[20:21], v[0:1], 2, s[8:9]
	global_load_dwordx3 v[0:2], v[20:21], off
	global_load_dword v6, v[10:11], off
	v_add_u32_e32 v7, 4, v18
	v_cmp_le_i32_e32 vcc, v7, v19
	s_waitcnt vmcnt(2)
	v_cvt_f32_f16_e32 v16, v22
	v_cvt_f32_f16_sdwa v17, v22 dst_sel:DWORD dst_unused:UNUSED_PAD src0_sel:WORD_1
	v_cvt_f32_f16_e32 v14, v23
	v_cvt_f32_f16_sdwa v15, v23 dst_sel:DWORD dst_unused:UNUSED_PAD src0_sel:WORD_1
	v_cvt_f32_f16_e32 v12, v24
	v_cvt_f32_f16_sdwa v13, v24 dst_sel:DWORD dst_unused:UNUSED_PAD src0_sel:WORD_1
	v_cvt_f32_f16_e32 v10, v25
	v_cvt_f32_f16_sdwa v11, v25 dst_sel:DWORD dst_unused:UNUSED_PAD src0_sel:WORD_1
	s_and_saveexec_b64 s[2:3], vcc
	s_xor_b64 s[2:3], exec, s[2:3]
	s_cbranch_execz .LBB3_4
	global_load_dword v9, v[20:21], off offset:12
	v_lshl_add_u64 v[20:21], v[20:21], 0, 16
	s_mov_b64 s[6:7], 0
	s_mov_b32 s8, 0xffff8
	v_mov_b32_e32 v7, -2
	.p2alignl 6, 3212836864
